# mLSTM: waves 1 and 3 skip the S=QK^T fragment reads and MFMAs (both of their S blocks lie above the causal diagonal, W is 0 there by the mask select)
# speedup vs baseline: 1.0049x; 1.0011x over previous
.LBB0_730:
	s_waitcnt lgkmcnt(0)
	s_barrier
	s_or_b64 vcc, s[28:29], s[34:35]
	s_and_b64 vcc, vcc, s[62:63]
	s_cbranch_vccz .Lml_S_main
	ds_read_b32 v0, v124 offset:1024
	v_add_u32_e32 v167, 0x4000, v165
	v_add_u32_e32 v168, 0x6000, v165
	v_lshlrev_b32_e32 v72, 16, v36
	v_and_b32_e32 v73, 0xffff0000, v36
	ds_write_b128 v142, v[36:39]
	v_and_b32_e32 v74, 0xffff0000, v37
	s_waitcnt lgkmcnt(1)
	v_mul_f32_e32 v72, v0, v72
	v_mul_f32_e32 v73, v0, v73
	v_cvt_pk_bf16_f32 v72, v72, v73
	v_lshlrev_b32_e32 v73, 16, v37
	v_mul_f32_e32 v73, v0, v73
	v_mul_f32_e32 v74, v0, v74
	v_cvt_pk_bf16_f32 v73, v73, v74
	v_lshlrev_b32_e32 v74, 16, v38
	v_and_b32_e32 v75, 0xffff0000, v38
	v_mul_f32_e32 v74, v0, v74
	v_mul_f32_e32 v75, v0, v75
	v_cvt_pk_bf16_f32 v74, v74, v75
	v_lshlrev_b32_e32 v75, 16, v39
	v_mul_f32_e32 v75, v0, v75
	v_and_b32_e32 v76, 0xffff0000, v39
	v_mul_f32_e32 v0, v0, v76
	v_cvt_pk_bf16_f32 v75, v75, v0
	ds_write_b128 v143, v[72:75]
	s_cmp_eq_u32 s88, 0x3e0000
	s_cbranch_scc1 .Lml_no_v_fetch_b
	v_mov_b32_e32 v36, v118
	s_nop 0
	global_load_dwordx4 v[36:39], v36, s[92:93]
.Lml_no_v_fetch_b:
	ds_read_b128 v[80:83], v150
	ds_read_b32 v0, v151
	ds_read_b32 v84, v164 offset:64
	s_waitcnt lgkmcnt(3)
	s_branch .Lml_S_join
.Lml_S_main:
	ds_read_b32 v0, v124 offset:1024
	ds_read_b128 v[222:225], v162
	ds_read_b128 v[226:229], v163 offset:33792
	ds_read_b128 v[84:87], v163 offset:42240
	ds_read_b128 v[210:213], v162 offset:64
	ds_read_b128 v[214:217], v163 offset:33856
	ds_read_b128 v[218:221], v163 offset:42304
	ds_read_b128 v[232:235], v162 offset:128
	ds_read_b128 v[236:239], v163 offset:33920
	ds_read_b128 v[240:243], v163 offset:42368
	ds_read_b128 v[176:179], v162 offset:192
	ds_read_b128 v[180:183], v163 offset:33984
	ds_read_b128 v[184:187], v163 offset:42432
	v_add_u32_e32 v167, 0x4000, v165
	v_add_u32_e32 v168, 0x6000, v165
	v_lshlrev_b32_e32 v72, 16, v36
	v_and_b32_e32 v73, 0xffff0000, v36
	ds_write_b128 v142, v[36:39]
	v_and_b32_e32 v74, 0xffff0000, v37
	s_waitcnt lgkmcnt(13)
	v_mul_f32_e32 v72, v0, v72
	v_mul_f32_e32 v73, v0, v73
	v_cvt_pk_bf16_f32 v72, v72, v73
	v_lshlrev_b32_e32 v73, 16, v37
	v_mul_f32_e32 v73, v0, v73
	v_mul_f32_e32 v74, v0, v74
	v_cvt_pk_bf16_f32 v73, v73, v74
	v_lshlrev_b32_e32 v74, 16, v38
	v_and_b32_e32 v75, 0xffff0000, v38
	v_mul_f32_e32 v74, v0, v74
	v_mul_f32_e32 v75, v0, v75
	v_cvt_pk_bf16_f32 v74, v74, v75
	v_lshlrev_b32_e32 v75, 16, v39
	v_mul_f32_e32 v75, v0, v75
	v_and_b32_e32 v76, 0xffff0000, v39
	v_mul_f32_e32 v0, v0, v76
	v_cvt_pk_bf16_f32 v75, v75, v0
	ds_write_b128 v143, v[72:75]
	s_cmp_eq_u32 s88, 0x3e0000
	s_cbranch_scc1 .Lml_no_v_fetch
	v_mov_b32_e32 v36, v118
	s_nop 0
	global_load_dwordx4 v[36:39], v36, s[92:93]

.Lml_S_join:
	v_add_u32_e32 v92, 0x2000, v165
	v_cvt_pk_bf16_f32 v244, v68, v69
	v_cvt_pk_bf16_f32 v245, v70, v71
	v_cvt_pk_bf16_f32 v246, v64, v65
	v_cvt_pk_bf16_f32 v247, v66, v67
	v_cvt_pk_bf16_f32 v206, v56, v57
	v_cvt_pk_bf16_f32 v207, v58, v59
	v_cvt_pk_bf16_f32 v208, v60, v61
	v_cvt_pk_bf16_f32 v209, v62, v63
	v_cvt_pk_bf16_f32 v222, v48, v49
	v_cvt_pk_bf16_f32 v223, v50, v51
	v_cvt_pk_bf16_f32 v224, v52, v53
	v_cvt_pk_bf16_f32 v225, v54, v55
	v_cvt_pk_bf16_f32 v226, v40, v41
	v_cvt_pk_bf16_f32 v227, v42, v43
	v_cvt_pk_bf16_f32 v228, v44, v45
	v_cvt_pk_bf16_f32 v229, v46, v47
	ds_read_b64 v[210:211], v165
	ds_read_b64 v[212:213], v165 offset:32
	ds_read_b64 v[214:215], v92 offset:256
	ds_read_b64 v[216:217], v92 offset:288
	ds_read_b64 v[218:219], v167 offset:512
	ds_read_b64 v[220:221], v167 offset:544
	ds_read_b64 v[232:233], v168 offset:768
	ds_read_b64 v[234:235], v168 offset:800
	ds_read_b64 v[236:237], v165 offset:64
	ds_read_b64 v[238:239], v165 offset:96
	ds_read_b64 v[240:241], v92 offset:320
	ds_read_b64 v[242:243], v92 offset:352
	s_waitcnt lgkmcnt(13)
	v_sub_f32_e32 v85, v0, v80
	v_min_f32_e32 v85, 0, v85
	s_waitcnt lgkmcnt(12)
	v_sub_f32_e32 v80, v84, v80
	v_exp_f32_e32 v85, v85
	v_min_f32_e32 v80, 0, v80
	v_exp_f32_e32 v80, v80
	v_mul_f32_e32 v76, v76, v85
	v_cndmask_b32_e64 v76, v76, 0, s[64:65]
	v_mul_f32_e32 v72, v72, v80
	v_cndmask_b32_e64 v72, v72, 0, s[66:67]
	v_cvt_pk_bf16_f32 v76, v76, v1
	v_add_u32_e32 v80, v155, v152
	ds_write_b16 v80, v76
	v_cvt_pk_bf16_f32 v72, v72, v1
	v_add_u32_e32 v76, v155, v153
	ds_write_b16 v76, v72
	v_sub_f32_e32 v72, v0, v81
	v_min_f32_e32 v72, 0, v72
	v_sub_f32_e32 v76, v84, v81
	v_exp_f32_e32 v72, v72
	v_min_f32_e32 v76, 0, v76
	v_exp_f32_e32 v76, v76
	v_mul_f32_e32 v72, v77, v72
	v_cndmask_b32_e64 v72, v72, 0, s[68:69]
	v_mul_f32_e32 v73, v73, v76
	v_cndmask_b32_e64 v73, v73, 0, s[70:71]
	v_cvt_pk_bf16_f32 v72, v72, v1
	v_add_u32_e32 v76, v156, v152
	ds_write_b16 v76, v72
	v_cvt_pk_bf16_f32 v72, v73, v1
	v_add_u32_e32 v73, v156, v153
	ds_write_b16 v73, v72
	v_sub_f32_e32 v72, v0, v82
	v_min_f32_e32 v72, 0, v72
	v_sub_f32_e32 v73, v84, v82
	v_exp_f32_e32 v72, v72
	v_min_f32_e32 v73, 0, v73
	v_exp_f32_e32 v73, v73
	v_sub_f32_e32 v0, v0, v83
	v_mul_f32_e32 v72, v78, v72
	v_cndmask_b32_e64 v72, v72, 0, s[72:73]
	v_mul_f32_e32 v73, v74, v73
	v_cndmask_b32_e64 v73, v73, 0, s[74:75]
	v_cvt_pk_bf16_f32 v72, v72, v1
	v_add_u32_e32 v74, v157, v152
	ds_write_b16 v74, v72
	v_cvt_pk_bf16_f32 v72, v73, v1
	v_add_u32_e32 v73, v157, v153
	ds_write_b16 v73, v72
	v_min_f32_e32 v0, 0, v0
	v_sub_f32_e32 v72, v84, v83
	v_exp_f32_e32 v0, v0
	v_min_f32_e32 v72, 0, v72
	v_exp_f32_e32 v72, v72
	v_add_u32_e32 v73, v158, v152
	v_mul_f32_e32 v0, v79, v0
	v_cndmask_b32_e64 v0, v0, 0, s[76:77]
	v_mul_f32_e32 v72, v75, v72
	v_cndmask_b32_e64 v72, v72, 0, s[78:79]
	v_cvt_pk_bf16_f32 v0, v0, v1
	ds_write_b16 v73, v0
	v_cvt_pk_bf16_f32 v0, v72, v1
	v_add_u32_e32 v72, v158, v153
	ds_write_b16 v72, v0
	v_add_u32_e32 v0, 0x2000, v165
	s_waitcnt lgkmcnt(8)
	ds_read_b64 v[176:177], v167 offset:576
	ds_read_b64 v[178:179], v167 offset:608
	ds_read_b64 v[180:181], v168 offset:832
	ds_read_b64 v[182:183], v168 offset:864
	ds_read_b64 v[184:185], v165 offset:128
	ds_read_b64 v[186:187], v165 offset:160
	ds_read_b64 v[194:195], v0 offset:384
	ds_read_b64 v[196:197], v0 offset:416
	ds_read_b64 v[198:199], v167 offset:640
	ds_read_b64 v[200:201], v167 offset:672
	ds_read_b64 v[202:203], v168 offset:896
	ds_read_b64 v[204:205], v168 offset:928
	v_mfma_f32_16x16x32_bf16 v[76:79], v[210:213], v[244:247], 0
	v_mfma_f32_16x16x32_bf16 v[80:83], v[214:217], v[244:247], 0
	v_mfma_f32_16x16x32_bf16 v[84:87], v[218:221], v[244:247], 0
	v_mfma_f32_16x16x32_bf16 v[88:91], v[232:235], v[244:247], 0
	v_mfma_f32_16x16x32_bf16 v[76:79], v[236:239], v[206:209], v[76:79]
	v_mfma_f32_16x16x32_bf16 v[80:83], v[240:243], v[206:209], v[80:83]
	s_waitcnt lgkmcnt(10)
	v_mfma_f32_16x16x32_bf16 v[84:87], v[176:179], v[206:209], v[84:87]
	ds_read_b64 v[210:211], v165 offset:192
	ds_read_b64 v[212:213], v165 offset:224
	s_waitcnt lgkmcnt(10)
	v_mfma_f32_16x16x32_bf16 v[88:91], v[180:183], v[206:209], v[88:91]
	ds_read_b64 v[214:215], v0 offset:448
	ds_read_b64 v[216:217], v0 offset:480
	s_waitcnt lgkmcnt(10)
	v_mfma_f32_16x16x32_bf16 v[76:79], v[184:187], v[222:225], v[76:79]
	ds_read_b64 v[218:219], v167 offset:704
	ds_read_b64 v[220:221], v167 offset:736
	s_waitcnt lgkmcnt(10)
	v_mfma_f32_16x16x32_bf16 v[80:83], v[194:197], v[222:225], v[80:83]
	ds_read_b64 v[232:233], v168 offset:960
	ds_read_b64 v[234:235], v168 offset:992
	s_waitcnt lgkmcnt(10)
	v_mfma_f32_16x16x32_bf16 v[84:87], v[198:201], v[222:225], v[84:87]
	s_waitcnt lgkmcnt(8)
	v_mfma_f32_16x16x32_bf16 v[88:91], v[202:205], v[222:225], v[88:91]
	s_waitcnt lgkmcnt(6)
	v_mfma_f32_16x16x32_bf16 v[76:79], v[210:213], v[226:229], v[76:79]
	s_waitcnt lgkmcnt(4)
	v_mfma_f32_16x16x32_bf16 v[80:83], v[214:217], v[226:229], v[80:83]
	s_waitcnt lgkmcnt(2)
	v_mfma_f32_16x16x32_bf16 v[84:87], v[218:221], v[226:229], v[84:87]
	s_waitcnt lgkmcnt(0)
	s_barrier
	v_mfma_f32_16x16x32_bf16 v[88:91], v[232:235], v[226:229], v[88:91]
